# late weight prep: transpose items moved to the workers that have no PEER-fold item (two or three per wave), fold-only on the rest
# speedup vs baseline: 1.0118x; 1.0011x over previous
; __device__ __forceinline__ void late_weight_prep(const Params& P, LAS unsigned char* lds, int lane, int wave, int gw, int NGW) {
;     ...
;         for (int it = gw; it < I_OUT + I_Q + I_O; it += NGW) {
;             int r = it;
;             if (r < I_OUT) { p0_transpose_item(P.w_out, 1024, 1024, 0, 32, (bf16*)(ws + WS_WOUT), 0, nullptr, scr, r, lane); continue; } r -= I_OUT;
;             if (r < I_Q) { p0_transpose_item(P.xattn_wq, 1024, 1024, 0, 32, (bf16*)(ws + WS_WQ), 0, P.norm_xattn_w, scr, r, lane); continue; } r -= I_Q;
;             p0_transpose_item(P.xattn_wo, 1024, 1024, 0, 32, (bf16*)(ws + WS_WO), 0, nullptr, scr, r, lane);
;         }
; __global__ void __launch_bounds__(NWAVES * 64, 2) hybrid_fwd(Params P) {
;     ...
;                 late_weight_prep(P, lds, lane, wave, w2 * NWAVES + wave, N2 * NWAVES);
.LBB0_1975:
	s_ashr_i32 s15, s14, 31
	s_cmpk_lt_i32 s16, 0x400
	s_cbranch_scc1 .LBB0_2008
	v_and_b32_e32 v1, 31, v0
	v_lshlrev_b32_e32 v20, 2, v1
	v_lshlrev_b32_e32 v1, 3, v0
	v_and_b32_e32 v1, 56, v1
	v_readlane_b32 s0, v254, 56
	v_lshlrev_b32_e32 v6, 1, v1
	v_mov_b32_e32 v7, 0
	s_mov_b32 s22, s0
	s_lshl_b32 s0, s0, 14
	v_lshrrev_b32_e32 v23, 3, v182
	v_lshl_add_u64 v[12:13], s[24:25], 0, v[6:7]
	s_mov_b64 s[6:7], 0x1200000
	v_readlane_b32 s44, v254, 40
	s_add_i32 s13, s0, 0
	v_lshrrev_b32_e32 v2, 5, v182
	v_mul_u32_u24_e32 v3, 0x84, v1
	v_lshl_add_u64 v[8:9], v[12:13], 0, s[6:7]
	v_lshlrev_b32_e32 v1, 2, v23
	s_mov_b64 s[6:7], 0xc00000
	v_readlane_b32 s45, v254, 41
	v_add3_u32 v44, s13, v3, v1
	v_lshl_add_u64 v[10:11], v[12:13], 0, s[6:7]
	s_mov_b64 s[6:7], 0xa00000
	s_cmp_lg_u64 s[44:45], 0
	v_mul_u32_u24_e32 v3, 0x84, v2
	v_lshl_add_u64 v[12:13], v[12:13], 0, s[6:7]
	v_mov_b32_e32 v21, v7
	v_readlane_b32 s52, v254, 48
	v_readlane_b32 s53, v254, 49
	v_readlane_b32 s54, v254, 50
	v_readlane_b32 s55, v254, 51
	v_readlane_b32 s56, v254, 52
	v_readlane_b32 s57, v254, 53
	v_readlane_b32 s58, v254, 54
	v_readlane_b32 s59, v254, 55
	s_cselect_b64 s[42:43], -1, 0
	v_or_b32_e32 v3, s0, v3
	s_lshl_b32 s0, s14, 8
	s_lshl_b32 s6, s22, 5
	v_add_u32_e32 v4, s13, v20
	v_lshl_add_u64 v[14:15], s[52:53], 0, v[20:21]
	v_readlane_b32 s52, v254, 24
	s_add_i32 s13, s0, s6
	s_add_i32 s13, s13, 0xffff8000
	s_lshl_b32 s0, s14, 4
	s_lshl_b32 s6, s22, 1
	v_readlane_b32 s1, v254, 57
	v_readlane_b32 s48, v254, 44
	v_readlane_b32 s49, v254, 45
	v_readlane_b32 s66, v254, 38
	v_readlane_b32 s67, v254, 39
	s_lshl_b32 s17, s26, 8
	s_add_i32 s0, s0, s6
	s_lshl_b32 s30, s26, 4
	s_mov_b32 s1, 0
	s_movk_i32 s3, 0x84
	v_or_b32_e32 v45, 8, v23
	v_or_b32_e32 v46, 16, v23
	v_or_b32_e32 v47, 24, v23
	v_lshl_add_u64 v[16:17], s[66:67], 0, v[20:21]
	v_mov_b32_e32 v1, v2
	v_add3_u32 v48, v3, v20, 0
	v_lshl_add_u64 v[20:21], s[48:49], 0, v[20:21]
	s_addk_i32 s17, 0xde00
	v_or_b32_e32 v49, 14, v2
	s_add_i32 s19, s0, 0x1f400
	s_addk_i32 s30, 0xfde0
	v_lshlrev_b32_e32 v22, 2, v2
	v_mov_b32_e32 v3, v7
	v_or_b32_e32 v50, 12, v2
	v_or_b32_e32 v51, 10, v2
	v_or_b32_e32 v52, 8, v2
	v_or_b32_e32 v53, 6, v2
	v_or_b32_e32 v54, 4, v2
	v_or_b32_e32 v55, 2, v2
	s_movk_i32 s31, 0x7fff
	s_mov_b32 s34, 0xffff0000
	s_add_i32 s35, s16, 0xfffffc00
	v_readlane_b32 s46, v254, 42
	v_readlane_b32 s47, v254, 43
	v_readlane_b32 s50, v254, 46
	v_readlane_b32 s51, v254, 47
	v_readlane_b32 s53, v254, 25
	v_readlane_b32 s54, v254, 26
	v_readlane_b32 s55, v254, 27
	v_readlane_b32 s56, v254, 28
	v_readlane_b32 s57, v254, 29
	v_readlane_b32 s58, v254, 30
	v_readlane_b32 s59, v254, 31
	v_readlane_b32 s60, v254, 32
	v_readlane_b32 s61, v254, 33
	v_readlane_b32 s62, v254, 34
	v_readlane_b32 s63, v254, 35
	v_readlane_b32 s64, v254, 36
	v_readlane_b32 s65, v254, 37
	s_branch .LBB0_1978
.LBB0_1977:
	s_addk_i32 s35, 0x2f0
	s_addk_i32 s13, 0x5e00
	s_addk_i32 s19, 0x5e0
	s_cmpk_gt_i32 s35, 0x5ff
	s_cbranch_scc1 .LBB0_2008
